# baseline (speedup 1.0000x reference)
.LBB2_9:
	s_lshr_b32 s8, s14, 7
	v_and_b32_e32 v1, 15, v0
	v_bfe_u32 v98, v0, 4, 2
	s_bfe_u32 s9, s14, 0x10006
	s_and_b64 vcc, exec, s[4:5]
	s_cbranch_vccz .LBB2_13
	s_barrier
	s_cmp_lt_i32 s6, 64
	s_mov_b32 s4, 0
	s_cbranch_scc1 .LBB2_41
	v_lshrrev_b32_e32 v2, 1, v0
	v_bfe_u32 v3, v0, 1, 3
	v_bitop3_b32 v2, v98, v2, 7 bitop3:0x78
	s_mul_i32 s5, s9, 0x60
	v_lshlrev_b32_e32 v99, 4, v2
	v_bitop3_b32 v2, v98, v3, 4 bitop3:0x36
	v_or_b32_e32 v4, s5, v1
	v_lshlrev_b32_e32 v102, 4, v2
	v_mov_b32_e32 v2, 0
	s_lshl_b32 s5, s8, 13
	v_lshlrev_b32_e32 v100, 7, v1
	v_lshlrev_b32_e32 v101, 7, v4
	v_mov_b32_e32 v3, v2
	v_mov_b32_e32 v4, v2
	v_mov_b32_e32 v5, v2
	v_mov_b32_e32 v6, v2
	v_mov_b32_e32 v7, v2
	v_mov_b32_e32 v8, v2
	v_mov_b32_e32 v9, v2
	v_mov_b32_e32 v34, v2
	v_mov_b32_e32 v35, v2
	v_mov_b32_e32 v36, v2
	v_mov_b32_e32 v37, v2
	v_mov_b32_e32 v38, v2
	v_mov_b32_e32 v39, v2
	v_mov_b32_e32 v40, v2
	v_mov_b32_e32 v41, v2
	v_mov_b32_e32 v66, v2
	v_mov_b32_e32 v67, v2
	v_mov_b32_e32 v68, v2
	v_mov_b32_e32 v69, v2
	v_mov_b32_e32 v70, v2
	v_mov_b32_e32 v71, v2
	v_mov_b32_e32 v72, v2
	v_mov_b32_e32 v73, v2
	v_mov_b32_e32 v10, v2
	v_mov_b32_e32 v11, v2
	v_mov_b32_e32 v12, v2
	v_mov_b32_e32 v13, v2
	v_mov_b32_e32 v14, v2
	v_mov_b32_e32 v15, v2
	v_mov_b32_e32 v16, v2
	v_mov_b32_e32 v17, v2
	v_mov_b32_e32 v42, v2
	v_mov_b32_e32 v43, v2
	v_mov_b32_e32 v44, v2
	v_mov_b32_e32 v45, v2
	v_mov_b32_e32 v46, v2
	v_mov_b32_e32 v47, v2
	v_mov_b32_e32 v48, v2
	v_mov_b32_e32 v49, v2
	v_mov_b32_e32 v74, v2
	v_mov_b32_e32 v75, v2
	v_mov_b32_e32 v76, v2
	v_mov_b32_e32 v77, v2
	v_mov_b32_e32 v78, v2
	v_mov_b32_e32 v79, v2
	v_mov_b32_e32 v80, v2
	v_mov_b32_e32 v81, v2
	v_mov_b32_e32 v18, v2
	v_mov_b32_e32 v19, v2
	v_mov_b32_e32 v20, v2
	v_mov_b32_e32 v21, v2
	v_mov_b32_e32 v22, v2
	v_mov_b32_e32 v23, v2
	v_mov_b32_e32 v24, v2
	v_mov_b32_e32 v25, v2
	v_mov_b32_e32 v50, v2
	v_mov_b32_e32 v51, v2
	v_mov_b32_e32 v52, v2
	v_mov_b32_e32 v53, v2
	v_mov_b32_e32 v54, v2
	v_mov_b32_e32 v55, v2
	v_mov_b32_e32 v56, v2
	v_mov_b32_e32 v57, v2
	v_mov_b32_e32 v82, v2
	v_mov_b32_e32 v83, v2
	v_mov_b32_e32 v84, v2
	v_mov_b32_e32 v85, v2
	v_mov_b32_e32 v86, v2
	v_mov_b32_e32 v87, v2
	v_mov_b32_e32 v88, v2
	v_mov_b32_e32 v89, v2
	v_mov_b32_e32 v26, v2
	v_mov_b32_e32 v27, v2
	v_mov_b32_e32 v28, v2
	v_mov_b32_e32 v29, v2
	v_mov_b32_e32 v30, v2
	v_mov_b32_e32 v31, v2
	v_mov_b32_e32 v32, v2
	v_mov_b32_e32 v33, v2
	v_mov_b32_e32 v58, v2
	v_mov_b32_e32 v59, v2
	v_mov_b32_e32 v60, v2
	v_mov_b32_e32 v61, v2
	v_mov_b32_e32 v62, v2
	v_mov_b32_e32 v63, v2
	v_mov_b32_e32 v64, v2
	v_mov_b32_e32 v65, v2
	v_mov_b32_e32 v90, v2
	v_mov_b32_e32 v91, v2
	v_mov_b32_e32 v92, v2
	v_mov_b32_e32 v93, v2
	v_mov_b32_e32 v94, v2
	v_mov_b32_e32 v95, v2
	v_mov_b32_e32 v96, v2
	v_mov_b32_e32 v97, v2
	v_add3_u32 v137, v99, s5, v100
	v_add_u32_e32 v138, v99, v101
	v_add3_u32 v139, v102, s5, v100
	v_add_u32_e32 v140, v102, v101
	s_mov_b32 s20, 0
	s_mul_i32 s6, s4, 0x6000
	s_add_i32 s6, s6, 0x10000
	v_add_u32_e32 v136, s20, v137
	v_add_u32_e32 v103, s6, v138
	v_add_u32_e32 v141, s20, v139
	v_add_u32_e32 v166, s6, v140
	ds_read_b128 v[112:115], v136
	ds_read_b128 v[116:119], v136 offset:2048
	ds_read_b128 v[142:145], v136 offset:4096
	ds_read_b128 v[146:149], v136 offset:6144
	ds_read_b128 v[104:107], v103 offset:32768
	ds_read_b128 v[108:111], v103 offset:34816
	ds_read_b128 v[120:123], v103 offset:36864
	ds_read_b128 v[124:127], v103 offset:38912
	ds_read_b128 v[128:131], v103 offset:40960
	ds_read_b128 v[132:135], v103 offset:43008
	.p2align	6
.LBB2_12:
	ds_read_b128 v[150:153], v141
	s_waitcnt lgkmcnt(6)
	v_mfma_f32_16x16x32_f16 v[94:97], v[104:107], v[112:115], v[94:97]
	v_mfma_f32_16x16x32_f16 v[86:89], v[104:107], v[116:119], v[86:89]
	v_mfma_f32_16x16x32_f16 v[78:81], v[104:107], v[142:145], v[78:81]
	v_mfma_f32_16x16x32_f16 v[70:73], v[104:107], v[146:149], v[70:73]
	ds_read_b128 v[104:107], v166 offset:32768
	ds_read_b128 v[154:157], v141 offset:2048
	s_waitcnt lgkmcnt(7)
	v_mfma_f32_16x16x32_f16 v[90:93], v[108:111], v[112:115], v[90:93]
	v_mfma_f32_16x16x32_f16 v[82:85], v[108:111], v[116:119], v[82:85]
	v_mfma_f32_16x16x32_f16 v[74:77], v[108:111], v[142:145], v[74:77]
	v_mfma_f32_16x16x32_f16 v[66:69], v[108:111], v[146:149], v[66:69]
	ds_read_b128 v[108:111], v166 offset:34816
	ds_read_b128 v[158:161], v141 offset:4096
	s_waitcnt lgkmcnt(8)
	v_mfma_f32_16x16x32_f16 v[62:65], v[120:123], v[112:115], v[62:65]
	v_mfma_f32_16x16x32_f16 v[54:57], v[120:123], v[116:119], v[54:57]
	v_mfma_f32_16x16x32_f16 v[46:49], v[120:123], v[142:145], v[46:49]
	v_mfma_f32_16x16x32_f16 v[38:41], v[120:123], v[146:149], v[38:41]
	ds_read_b128 v[120:123], v166 offset:36864
	ds_read_b128 v[162:165], v141 offset:6144
	s_waitcnt lgkmcnt(9)
	v_mfma_f32_16x16x32_f16 v[58:61], v[124:127], v[112:115], v[58:61]
	v_mfma_f32_16x16x32_f16 v[50:53], v[124:127], v[116:119], v[50:53]
	v_mfma_f32_16x16x32_f16 v[42:45], v[124:127], v[142:145], v[42:45]
	v_mfma_f32_16x16x32_f16 v[34:37], v[124:127], v[146:149], v[34:37]
	ds_read_b128 v[124:127], v166 offset:38912
	s_waitcnt lgkmcnt(9)
	v_mfma_f32_16x16x32_f16 v[30:33], v[128:131], v[112:115], v[30:33]
	v_mfma_f32_16x16x32_f16 v[22:25], v[128:131], v[116:119], v[22:25]
	v_mfma_f32_16x16x32_f16 v[14:17], v[128:131], v[142:145], v[14:17]
	v_mfma_f32_16x16x32_f16 v[6:9], v[128:131], v[146:149], v[6:9]
	ds_read_b128 v[128:131], v166 offset:40960
	s_waitcnt lgkmcnt(9)
	v_mfma_f32_16x16x32_f16 v[26:29], v[132:135], v[112:115], v[26:29]
	v_mfma_f32_16x16x32_f16 v[18:21], v[132:135], v[116:119], v[18:21]
	v_mfma_f32_16x16x32_f16 v[10:13], v[132:135], v[142:145], v[10:13]
	v_mfma_f32_16x16x32_f16 v[2:5], v[132:135], v[146:149], v[2:5]
	ds_read_b128 v[132:135], v166 offset:43008
	s_waitcnt lgkmcnt(3)
	v_mfma_f32_16x16x32_f16 v[94:97], v[104:107], v[150:153], v[94:97]
	v_mfma_f32_16x16x32_f16 v[86:89], v[104:107], v[154:157], v[86:89]
	v_mfma_f32_16x16x32_f16 v[78:81], v[104:107], v[158:161], v[78:81]
	v_mfma_f32_16x16x32_f16 v[70:73], v[104:107], v[162:165], v[70:73]
	v_mfma_f32_16x16x32_f16 v[90:93], v[108:111], v[150:153], v[90:93]
	v_mfma_f32_16x16x32_f16 v[82:85], v[108:111], v[154:157], v[82:85]
	v_mfma_f32_16x16x32_f16 v[74:77], v[108:111], v[158:161], v[74:77]
	v_mfma_f32_16x16x32_f16 v[66:69], v[108:111], v[162:165], v[66:69]
	v_mfma_f32_16x16x32_f16 v[62:65], v[120:123], v[150:153], v[62:65]
	v_mfma_f32_16x16x32_f16 v[54:57], v[120:123], v[154:157], v[54:57]
	v_mfma_f32_16x16x32_f16 v[46:49], v[120:123], v[158:161], v[46:49]
	v_mfma_f32_16x16x32_f16 v[38:41], v[120:123], v[162:165], v[38:41]
	s_waitcnt lgkmcnt(0)
	s_barrier
	s_add_i32 s4, s4, 1
	s_cmp_lg_u32 s4, 2
	s_cselect_b32 s4, s4, 0
	s_add_i32 s20, s20, 0x8000
	s_cmp_lg_u32 s20, 0x18000
	s_cselect_b32 s20, s20, 0
	s_mul_i32 s6, s4, 0x6000
	s_add_i32 s6, s6, 0x10000
	v_add_u32_e32 v136, s20, v137
	v_add_u32_e32 v103, s6, v138
	v_add_u32_e32 v141, s20, v139
	v_add_u32_e32 v166, s6, v140
	ds_read_b128 v[112:115], v136
	ds_read_b128 v[116:119], v136 offset:2048
	ds_read_b128 v[142:145], v136 offset:4096
	ds_read_b128 v[146:149], v136 offset:6144
	ds_read_b128 v[104:107], v103 offset:32768
	ds_read_b128 v[108:111], v103 offset:34816
	ds_read_b128 v[120:123], v103 offset:36864
	v_mfma_f32_16x16x32_f16 v[58:61], v[124:127], v[150:153], v[58:61]
	v_mfma_f32_16x16x32_f16 v[50:53], v[124:127], v[154:157], v[50:53]
	v_mfma_f32_16x16x32_f16 v[42:45], v[124:127], v[158:161], v[42:45]
	v_mfma_f32_16x16x32_f16 v[34:37], v[124:127], v[162:165], v[34:37]
	ds_read_b128 v[124:127], v103 offset:38912
	v_mfma_f32_16x16x32_f16 v[30:33], v[128:131], v[150:153], v[30:33]
	v_mfma_f32_16x16x32_f16 v[22:25], v[128:131], v[154:157], v[22:25]
	v_mfma_f32_16x16x32_f16 v[14:17], v[128:131], v[158:161], v[14:17]
	v_mfma_f32_16x16x32_f16 v[6:9], v[128:131], v[162:165], v[6:9]
	ds_read_b128 v[128:131], v103 offset:40960
	v_mfma_f32_16x16x32_f16 v[26:29], v[132:135], v[150:153], v[26:29]
	v_mfma_f32_16x16x32_f16 v[18:21], v[132:135], v[154:157], v[18:21]
	v_mfma_f32_16x16x32_f16 v[10:13], v[132:135], v[158:161], v[10:13]
	v_mfma_f32_16x16x32_f16 v[2:5], v[132:135], v[162:165], v[2:5]
	ds_read_b128 v[132:135], v103 offset:43008
	s_add_i32 s7, s7, -1
	s_cmp_lg_u32 s7, 0
	s_cbranch_scc1 .LBB2_12
	s_branch .LBB2_14

	.amdhsa_kernel _Z7gemm_dbILi256ELi192ELi64ELi96ELi64ELi2ELi1ELi4EEvPKDF16_S1_PfPDF16_S3_S3_PK15HIP_vector_typeIfLj2EEiii
		.amdhsa_group_segment_fixed_size 32768
		.amdhsa_private_segment_fixed_size 0
		.amdhsa_kernarg_size 68
		.amdhsa_user_sgpr_count 2
		.amdhsa_user_sgpr_dispatch_ptr 0
		.amdhsa_user_sgpr_queue_ptr 0
		.amdhsa_user_sgpr_kernarg_segment_ptr 1
		.amdhsa_user_sgpr_dispatch_id 0
		.amdhsa_user_sgpr_kernarg_preload_length 0
		.amdhsa_user_sgpr_kernarg_preload_offset 0
		.amdhsa_user_sgpr_private_segment_size 0
		.amdhsa_uses_dynamic_stack 0
		.amdhsa_enable_private_segment 0
		.amdhsa_system_sgpr_workgroup_id_x 1
		.amdhsa_system_sgpr_workgroup_id_y 0
		.amdhsa_system_sgpr_workgroup_id_z 0
		.amdhsa_system_sgpr_workgroup_info 0
		.amdhsa_system_vgpr_workitem_id 0
		.amdhsa_next_free_vgpr 168
		.amdhsa_next_free_sgpr 21
		.amdhsa_accum_offset 168
		.amdhsa_reserve_vcc 1
		.amdhsa_float_round_mode_32 0
		.amdhsa_float_round_mode_16_64 0
		.amdhsa_float_denorm_mode_32 3
		.amdhsa_float_denorm_mode_16_64 3
		.amdhsa_dx10_clamp 1
		.amdhsa_ieee_mode 1
		.amdhsa_fp16_overflow 0
		.amdhsa_tg_split 0
		.amdhsa_exception_fp_ieee_invalid_op 0
		.amdhsa_exception_fp_denorm_src 0
		.amdhsa_exception_fp_ieee_div_zero 0
		.amdhsa_exception_fp_ieee_overflow 0
		.amdhsa_exception_fp_ieee_underflow 0
		.amdhsa_exception_fp_ieee_inexact 0
		.amdhsa_exception_int_div_zero 0
	.end_amdhsa_kernel

amdhsa.kernels:
  - .agpr_count:     0
    .args:
      - .actual_access:  read_only
        .address_space:  global
        .offset:         0
        .size:           8
        .value_kind:     global_buffer
      - .actual_access:  read_only
        .address_space:  global
        .offset:         8
        .size:           8
        .value_kind:     global_buffer
      - .actual_access:  read_only
        .address_space:  global
        .offset:         16
        .size:           8
        .value_kind:     global_buffer
      - .actual_access:  read_only
        .address_space:  global
        .offset:         24
        .size:           8
        .value_kind:     global_buffer
      - .actual_access:  read_only
        .address_space:  global
        .offset:         32
        .size:           8
        .value_kind:     global_buffer
      - .address_space:  global
        .offset:         40
        .size:           8
        .value_kind:     global_buffer
      - .address_space:  global
        .offset:         48
        .size:           8
        .value_kind:     global_buffer
      - .address_space:  global
        .offset:         56
        .size:           8
        .value_kind:     global_buffer
      - .address_space:  global
        .offset:         64
        .size:           8
        .value_kind:     global_buffer
    .group_segment_fixed_size: 0
    .kernarg_segment_align: 8
    .kernarg_segment_size: 72
    .language:       OpenCL C
    .language_version:
      - 2
      - 0
    .max_flat_workgroup_size: 256
    .name:           _Z11prep_kernelPKfS0_S0_S0_S0_PDF16_S1_S1_P15HIP_vector_typeIfLj2EE
    .private_segment_fixed_size: 0
    .sgpr_count:     22
    .sgpr_spill_count: 0
    .symbol:         _Z11prep_kernelPKfS0_S0_S0_S0_PDF16_S1_S1_P15HIP_vector_typeIfLj2EE.kd
    .uniform_work_group_size: 1
    .uses_dynamic_stack: false
    .vgpr_count:     20
    .vgpr_spill_count: 0
    .wavefront_size: 64
  - .agpr_count:     0
    .args:
      - .address_space:  global
        .offset:         0
        .size:           8
        .value_kind:     global_buffer
      - .address_space:  global
        .offset:         8
        .size:           8
        .value_kind:     global_buffer
      - .address_space:  global
        .offset:         16
        .size:           8
        .value_kind:     global_buffer
      - .address_space:  global
        .offset:         24
        .size:           8
        .value_kind:     global_buffer
    .group_segment_fixed_size: 0
    .kernarg_segment_align: 8
    .kernarg_segment_size: 32
    .language:       OpenCL C
    .language_version:
      - 2
      - 0
    .max_flat_workgroup_size: 512
    .name:           _Z10attn64_fwdPKDF16_S0_S0_PDF16_
    .private_segment_fixed_size: 0
    .sgpr_count:     48
    .sgpr_spill_count: 0
    .symbol:         _Z10attn64_fwdPKDF16_S0_S0_PDF16_.kd
    .uniform_work_group_size: 1
    .uses_dynamic_stack: false
    .vgpr_count:     252
    .vgpr_spill_count: 0
    .wavefront_size: 64
  - .agpr_count:     0
    .args:
      - .address_space:  global
        .offset:         0
        .size:           8
        .value_kind:     global_buffer
      - .address_space:  global
        .offset:         8
        .size:           8
        .value_kind:     global_buffer
      - .address_space:  global
        .offset:         16
        .size:           8
        .value_kind:     global_buffer
      - .address_space:  global
        .offset:         24
        .size:           8
        .value_kind:     global_buffer
      - .address_space:  global
        .offset:         32
        .size:           8
        .value_kind:     global_buffer
      - .address_space:  global
        .offset:         40
        .size:           8
        .value_kind:     global_buffer
      - .actual_access:  read_only
        .address_space:  global
        .offset:         48
        .size:           8
        .value_kind:     global_buffer
      - .offset:         56
        .size:           4
        .value_kind:     by_value
      - .offset:         60
        .size:           4
        .value_kind:     by_value
      - .offset:         64
        .size:           4
        .value_kind:     by_value
    .group_segment_fixed_size: 32768
    .kernarg_segment_align: 8
    .kernarg_segment_size: 68
    .language:       OpenCL C
    .language_version:
      - 2
      - 0
    .max_flat_workgroup_size: 768
    .name:           _Z7gemm_dbILi256ELi192ELi64ELi96ELi64ELi2ELi1ELi4EEvPKDF16_S1_PfPDF16_S3_S3_PK15HIP_vector_typeIfLj2EEiii
    .private_segment_fixed_size: 0
    .sgpr_count:     27
    .sgpr_spill_count: 0
    .symbol:         _Z7gemm_dbILi256ELi192ELi64ELi96ELi64ELi2ELi1ELi4EEvPKDF16_S1_PfPDF16_S3_S3_PK15HIP_vector_typeIfLj2EEiii.kd
    .uniform_work_group_size: 1
    .uses_dynamic_stack: false
    .vgpr_count:     168
    .vgpr_spill_count: 0
    .wavefront_size: 64
  - .agpr_count:     0
    .args:
      - .address_space:  global
        .offset:         0
        .size:           8
        .value_kind:     global_buffer
      - .address_space:  global
        .offset:         8
        .size:           8
        .value_kind:     global_buffer
      - .address_space:  global
        .offset:         16
        .size:           8
        .value_kind:     global_buffer
      - .address_space:  global
        .offset:         24
        .size:           8
        .value_kind:     global_buffer
      - .address_space:  global
        .offset:         32
        .size:           8
        .value_kind:     global_buffer
      - .address_space:  global
        .offset:         40
        .size:           8
        .value_kind:     global_buffer
      - .actual_access:  read_only
        .address_space:  global
        .offset:         48
        .size:           8
        .value_kind:     global_buffer
      - .offset:         56
        .size:           4
        .value_kind:     by_value
      - .offset:         60
        .size:           4
        .value_kind:     by_value
      - .offset:         64
        .size:           4
        .value_kind:     by_value
    .group_segment_fixed_size: 0
    .kernarg_segment_align: 8
    .kernarg_segment_size: 68
    .language:       OpenCL C
    .language_version:
      - 2
      - 0
    .max_flat_workgroup_size: 512
    .name:           _Z7gemm_dbILi128ELi128ELi64ELi64ELi64ELi3ELi0ELi4EEvPKDF16_S1_PfPDF16_S3_S3_PK15HIP_vector_typeIfLj2EEiii
    .private_segment_fixed_size: 0
    .sgpr_count:     26
    .sgpr_spill_count: 0
    .symbol:         _Z7gemm_dbILi128ELi128ELi64ELi64ELi64ELi3ELi0ELi4EEvPKDF16_S1_PfPDF16_S3_S3_PK15HIP_vector_typeIfLj2EEiii.kd
    .uniform_work_group_size: 1
    .uses_dynamic_stack: false
    .vgpr_count:     168
    .vgpr_spill_count: 0
    .wavefront_size: 64
